# all expert-weight conversion done inside the MLA attention tile loop (64x32 chunks, 64-B store pieces), work queue disabled
# baseline (speedup 1.0000x reference)
; #define LAS __attribute__((address_space(3)))
; __device__ __forceinline__ int hw_wave_slot() { return (int)(__builtin_amdgcn_s_getreg((5 << 11) | 4) & 63u); }
; __device__ __forceinline__ unsigned xb_add(unsigned* p, unsigned v) { return __hip_atomic_fetch_add(p, v, __ATOMIC_RELAXED, __HIP_MEMORY_SCOPE_AGENT); }
; __device__ __forceinline__ unsigned xb_xcc_id() { return (unsigned)__builtin_amdgcn_s_getreg((3 << 11) | 20) & 0xFu; }
;     __device__ __forceinline__ unsigned char* ws() const { return *(unsigned char* const __attribute__((address_space(4)))*)(p + 232); }
; __device__ __forceinline__ KA fresh_ka() { kaptr p = (kaptr)__builtin_amdgcn_kernarg_segment_ptr(); asm volatile("" : "+s"(p)); return KA{p}; }
; __device__ __forceinline__ XcdBarrier xcd_barrier_post(unsigned* bar, volatile LAS unsigned* st) {
;     XcdBarrier b; b.bar = bar; b.x = xb_xcc_id(); b.st = st;
;     if (tid_x() == 0) (void)xb_add(&bar[XB_XCNT(b.x)], 1u);
;     return b;
; __global__ void __launch_bounds__(512, 2) mk_fwd(Args args) {
;     ...
;     {
;         const KA a = fresh_ka(); unsigned char* ws = a.ws();
;         LAS unsigned char* lds = (LAS unsigned char*)lds_raw;
;         for (int u = threadIdx.x; u < 128; u += 512) ((LAS unsigned*)(lds + MISC_OFF))[u] = 0u;
;         __syncthreads();
;         if ((threadIdx.x & 63) == 0) ((LAS int*)(lds + MISC_OFF))[64 + hw_wave_slot()] = (int)(threadIdx.x >> 6);
;         __syncthreads();
;         unsigned* ctl = (unsigned*)(ws + WS_CTL);
;         bar.bar = ctl + CW_BAR; bar.x = 0; bar.st = (volatile LAS unsigned*)(lds + MISC_OFF) + 8;
;         if (!MK_PER_PHASE) bar = xcd_barrier_post(ctl + CW_BAR, (volatile LAS unsigned*)(lds + MISC_OFF) + 8);
.LBB0_4:
	s_or_b64 exec, exec, s[4:5]
	s_add_u32 s78, s2, 0x4000
	s_waitcnt lgkmcnt(0)
	s_barrier
	s_addc_u32 s79, s3, 0
	s_getreg_b32 s2, hwreg(HW_REG_XCC_ID, 0, 4)
	s_getreg_b32 s3, hwreg(HW_REG_HW_ID, 0, 6)
	s_and_b32 s3, s3, 63
	s_lshl_b32 s3, s3, 2
	s_add_i32 s3, s3, 0
	s_add_i32 s3, s3, 0x23f00
	v_mov_b32_e32 v0, s3
	ds_read_b32 v0, v0
	s_and_b32 s30, s2, 15
	v_mbcnt_lo_u32_b32 v1, -1, 0
	v_mbcnt_hi_u32_b32 v1, -1, v1
	s_waitcnt lgkmcnt(0)
	v_readfirstlane_b32 s2, v0
	s_lshl_b32 s2, s2, 6
	v_sub_u32_e32 v0, 0, v1
	v_cmp_eq_u32_e32 vcc, s2, v0
	s_and_saveexec_b64 s[2:3], vcc
	s_cbranch_execz .LBB0_7
	s_mov_b64 s[4:5], exec
	v_mbcnt_lo_u32_b32 v0, s4, 0
	v_mbcnt_hi_u32_b32 v0, s5, v0
	v_cmp_eq_u32_e32 vcc, 0, v0
	s_and_b64 s[6:7], exec, vcc
	s_mov_b64 exec, s[6:7]
	s_cbranch_execz .LBB0_7
	s_lshl_b32 s6, s30, 8
	s_bcnt1_i32_b64 s4, s[4:5]
	v_mov_b32_e32 v0, s6
	v_mov_b32_e32 v1, s4
	global_atomic_add v0, v1, s[78:79] offset:1024
	v_mov_b32_e32 v0, 0x1c000
	v_mov_b32_e32 v1, 0x18600
	global_atomic_add v0, v1, s[78:79]

;     ...
;     int tid = tid_x(); asm volatile("" : "+v"(tid));
;     const int wid = tid >> 6, lane = tid & 63, r32 = lane & 31, hi = lane >> 5;
;     const int qb = uid & 15, h = (uid >> 4) % NH, b = (uid >> 4) / NH;
;     const int tok0 = b * SEQ;
;     const int qrow = tok0 + qb * 256 + wid * 32 + r32;
;     LAS char* V_lds = lds + LDS_VBUF; LAS char* K_lds = lds + LDS_KBUF;
;     LAS float* ws = (LAS float*)(lds + LDS_WS) + wid * 64; LAS float* li_l = ws; LAS float* al_l = ws + 32;
;     LAS float* rpbL = (LAS float*)(lds + LDS_RPB);
;     const int sr = tid >> 4, sc = (tid & 15) * 8, vst0 = v_st(sr, sc), vst1 = v_st(32 + sr, sc);
;     const int sr64 = tid >> 3, sc64 = (tid & 7) * 8;
;     const int vb0 = (int)(unsigned)(uintptr_t)V_lds + v_rd_base(lane);
;     int NT = 64, kbase = tok0;
;     int rq = 0, qc = 0, kr_lo = 0;
;     if constexpr (MODE == MODE_NA) { const int rq0 = qb * 4; kr_lo = min(min(max(rq0 - 4, 0), 56), 52); NT = 12; kbase = tok0 + kr_lo * 64; rq = rq0 + (wid >> 1); qc = (wid & 1) * 32 + r32;
;         for (int i = tid; i < 15 * 31; i += 512) rpbL[i] = P.rpb[h * 465 + i];
;         __syncthreads(); }
;     const bf16* Kg; const bf16* Vg; const bf16* Kg2 = nullptr; int ldk, ldv;
;     if constexpr (MODE == MODE_MLA) { Kg = P.KVM + h * 256; Vg = P.KVM + h * 256 + 128; Kg2 = P.U + U_KR; ldk = KVW; ldv = KVW; }
;     else if constexpr (MODE == MODE_NA) { Kg = P.U + U_NA + 512 + h * 128; Vg = P.U + U_NA + 1024 + h * 128; ldk = UW; ldv = UW; }
;     else { Kg = P.U + U_DF + 512 + h * 128; Vg = P.U + U_DF + 1024 + h * 128; ldk = UW; ldv = UW; }
;     constexpr int pass = PASS;
;     constexpr bool HALF_OFFSET = false;
;     {
;         float m_reg = -1e30f, l_reg = 0; f32x16 o[4] = {}; bf16x8 qr[NQ];
;         if constexpr (MODE == MODE_MLA) {
;             const bf16* Qw = P.QM + (size_t)qrow * QMW + h * 192 + hi * 8;
; #pragma unroll
;             for (int d0 = 0; d0 < 12; ++d0) qr[d0] = *(const bf16x8*)(Qw + d0 * 16);
;             const f32x2* rt = P.ropeM + (size_t)(qrow & (SEQ - 1)) * 32;
; #pragma unroll
;             for (int g = 0; g < 2; ++g) {
;                 bf16x8 x1 = qr[8 + g], x2 = qr[10 + g];
; #pragma unroll
;                 for (int e = 0; e < 8; ++e) { const f32x2 cs = rt[g * 16 + hi * 8 + e];
;                     const float a = bf2f((unsigned short)x1[e]), c = bf2f((unsigned short)x2[e]);
.LBB0_785:
	s_lshl_b32 s0, s22, 1
	s_and_b32 s0, s0, 14
	s_ashr_i32 s1, s22, 7
	s_add_i32 s0, s0, s1
	s_getreg_b32 s1, hwreg(HW_REG_HW_ID, 0, 6)
	s_and_b32 s1, s1, 63
	s_lshl_b32 s1, s1, 2
	s_add_i32 s1, s1, 0
	s_add_i32 s1, s1, 0x23f00
	s_waitcnt vmcnt(15)
	v_mov_b32_e32 v0, s1
	ds_read_b32 v0, v0
	v_mbcnt_lo_u32_b32 v1, -1, 0
	v_mbcnt_hi_u32_b32 v1, -1, v1
	v_mov_b32_e32 v145, v193
	v_mov_b32_e32 v149, v193
	s_movk_i32 s3, 0x70
	s_waitcnt lgkmcnt(0)
	v_readfirstlane_b32 s1, v0
	s_mov_b32 s28, 0
	s_and_b32 s39, s74, 63
	s_lshl_b32 s39, s39, 3
	s_add_u32 s39, s39, s1
	s_lshr_b32 s54, s74, 6
	v_lshrrev_b32_e32 v226, 3, v1
	v_and_b32_e32 v229, 7, v1
	v_readlane_b32 s56, v254, 60
	s_mov_b32 s42, 0
	v_mov_b32_e32 v147, v193
	s_waitcnt vmcnt(13)
	v_lshl_add_u32 v11, s1, 6, v1
	s_lshr_b32 s1, s0, 29
	s_add_i32 s1, s0, s1
	s_and_b32 s2, s1, -8
	s_sub_i32 s23, s0, s2
	s_lshl_b32 s0, s1, 9
	s_and_b32 s4, s0, 0xfffff000
	s_lshl_b32 s0, s22, 5
	s_and_b32 s0, s0, 0xf00
	s_or_b32 s25, s4, s0
	v_ashrrev_i32_e32 v156, 6, v11
	v_and_b32_e32 v154, 31, v11
	v_lshl_add_u32 v0, v156, 5, s25
	v_or_b32_e32 v8, v0, v154
	v_and_b32_e32 v0, 0x3fffffc0, v11
	s_add_i32 s0, 0, 0x1e000
	v_lshl_add_u32 v157, v0, 2, s0
	s_lshl_b32 s0, s23, 8
	s_ashr_i32 s1, s0, 31
	s_lshl_b64 s[0:1], s[0:1], 1
	s_add_u32 s26, s18, s0
	v_mov_b64_e32 v[0:1], s[10:11]
	s_movk_i32 s0, 0xc00
	s_addc_u32 s27, s19, s1
	v_mad_i64_i32 v[0:1], s[0:1], v8, s0, v[0:1]
	s_mul_i32 s0, s23, 0xc0
	v_lshlrev_b32_e32 v8, 8, v8
	v_bfe_u32 v155, v11, 5, 1
	s_ashr_i32 s1, s0, 31
	v_and_b32_e32 v192, 0xfff00, v8
	v_lshl_add_u64 v[0:1], s[0:1], 1, v[0:1]
	v_lshlrev_b32_e32 v144, 4, v155
	v_lshl_add_u64 v[8:9], s[12:13], 0, v[192:193]
	v_lshlrev_b32_e32 v192, 6, v155
	v_lshl_add_u64 v[4:5], v[0:1], 0, v[144:145]
	v_lshl_add_u64 v[8:9], v[8:9], 0, v[192:193]
	global_load_dwordx4 v[96:99], v[4:5], off
	global_load_dwordx4 v[100:103], v[4:5], off offset:32
	global_load_dwordx4 v[104:107], v[4:5], off offset:64
	global_load_dwordx4 v[108:111], v[4:5], off offset:96
	global_load_dwordx4 v[112:115], v[4:5], off offset:128
	global_load_dwordx4 v[116:119], v[4:5], off offset:160
	global_load_dwordx4 v[120:123], v[4:5], off offset:192
	global_load_dwordx4 v[124:127], v[4:5], off offset:224
	global_load_dwordx4 v[26:29], v[4:5], off offset:256
	global_load_dwordx4 v[0:3], v[4:5], off offset:288
	global_load_dwordx4 v[30:33], v[4:5], off offset:320
	s_nop 0
	global_load_dwordx4 v[4:7], v[4:5], off offset:352
	s_waitcnt vmcnt(24)
	v_lshlrev_b32_e32 v13, 4, v11
	global_load_dwordx2 v[14:15], v[8:9], off
	v_readfirstlane_b32 s0, v156
	s_ashr_i32 s5, s4, 31
	s_lshl_b32 s2, s0, 10
	s_lshl_b64 s[0:1], s[4:5], 12
	s_add_u32 s0, s26, s0
	s_addc_u32 s1, s27, s1
	s_add_i32 s29, s2, 0
	s_mov_b32 m0, s29
	s_add_i32 s2, s29, 0xc000
	v_and_b32_e32 v10, 63, v11
	v_and_b32_e32 v12, 0xc0, v13
	v_mov_b32_e32 v151, v193
	v_lshlrev_b32_e32 v145, 8, v154
	v_lshlrev_b32_e32 v167, 7, v154
	v_lshl_add_u32 v163, v154, 2, v157
	v_mov_b32_e32 v174, 0
	v_mov_b32_e32 v173, 0xf149f2ca
	s_waitcnt vmcnt(4)
	v_lshlrev_b32_e32 v17, 16, v26
	s_waitcnt vmcnt(2)
	v_lshlrev_b32_e32 v16, 16, v30
	s_waitcnt vmcnt(0)
	v_pk_mul_f32 v[18:19], v[14:15], v[16:17] op_sel:[0,1] op_sel_hi:[1,0]
	v_pk_mul_f32 v[14:15], v[14:15], v[16:17]
	v_sub_f32_e32 v18, v18, v19
	v_add_f32_e32 v14, v15, v14
	v_cvt_pk_bf16_f32 v15, v18, v193
	v_cvt_pk_bf16_f32 v14, v14, v193
	global_load_dwordx2 v[16:17], v[8:9], off offset:8
	v_and_b32_e32 v19, 0xffff0000, v26
	v_and_b32_e32 v18, 0xffff0000, v30
	s_waitcnt vmcnt(0)
	v_pk_mul_f32 v[20:21], v[16:17], v[18:19] op_sel:[0,1] op_sel_hi:[1,0]
	v_pk_mul_f32 v[16:17], v[16:17], v[18:19]
	v_sub_f32_e32 v20, v20, v21
	v_add_f32_e32 v16, v16, v17
	v_cvt_pk_bf16_f32 v17, v20, v193
	v_cvt_pk_bf16_f32 v16, v16, v193
	global_load_dwordx2 v[18:19], v[8:9], off offset:16
	v_lshlrev_b32_e32 v21, 16, v27
	v_lshlrev_b32_e32 v20, 16, v31
	s_waitcnt vmcnt(0)
	v_pk_mul_f32 v[22:23], v[18:19], v[20:21] op_sel:[0,1] op_sel_hi:[1,0]
	v_pk_mul_f32 v[18:19], v[18:19], v[20:21]
	v_sub_f32_e32 v22, v22, v23
	v_add_f32_e32 v18, v18, v19
	v_cvt_pk_bf16_f32 v19, v22, v193
	v_cvt_pk_bf16_f32 v18, v18, v193
	global_load_dwordx2 v[20:21], v[8:9], off offset:24
	v_and_b32_e32 v23, 0xffff0000, v27
	v_and_b32_e32 v22, 0xffff0000, v31
	s_waitcnt vmcnt(0)
	v_pk_mul_f32 v[24:25], v[20:21], v[22:23] op_sel:[0,1] op_sel_hi:[1,0]
	v_pk_mul_f32 v[20:21], v[20:21], v[22:23]
	v_sub_f32_e32 v24, v24, v25
	v_add_f32_e32 v20, v20, v21
	v_cvt_pk_bf16_f32 v21, v24, v193
	v_cvt_pk_bf16_f32 v20, v20, v193
	global_load_dwordx2 v[22:23], v[8:9], off offset:32
	v_lshlrev_b32_e32 v25, 16, v28
	v_lshlrev_b32_e32 v24, 16, v32
	s_waitcnt vmcnt(0)
	v_pk_mul_f32 v[26:27], v[22:23], v[24:25] op_sel:[0,1] op_sel_hi:[1,0]
	v_pk_mul_f32 v[22:23], v[22:23], v[24:25]
	v_sub_f32_e32 v26, v26, v27
	v_add_f32_e32 v22, v22, v23
	v_cvt_pk_bf16_f32 v23, v26, v193
	v_cvt_pk_bf16_f32 v22, v22, v193
	global_load_dwordx2 v[24:25], v[8:9], off offset:40
	v_and_b32_e32 v27, 0xffff0000, v28
	v_and_b32_e32 v26, 0xffff0000, v32
	s_waitcnt vmcnt(0)
	v_pk_mul_f32 v[30:31], v[24:25], v[26:27] op_sel:[0,1] op_sel_hi:[1,0]
	v_pk_mul_f32 v[24:25], v[24:25], v[26:27]
	v_sub_f32_e32 v28, v30, v31
	v_add_f32_e32 v24, v24, v25
	v_cvt_pk_bf16_f32 v25, v28, v193
	v_cvt_pk_bf16_f32 v24, v24, v193
	global_load_dwordx2 v[26:27], v[8:9], off offset:48
	v_lshlrev_b32_e32 v31, 16, v29
	v_lshlrev_b32_e32 v30, 16, v33
	v_and_b32_e32 v29, 0xffff0000, v29
	s_waitcnt vmcnt(0)
; __device__ __forceinline__ unsigned cvt_pk_bf16(float lo, float hi) { unsigned r; asm volatile("v_cvt_pk_bf16_f32 %0, %1, %2" : "=v"(r) : "v"(lo), "v"(hi)); return r; }
;     ...
; #pragma unroll
;             for (int g = 0; g < 2; ++g) {
;                 bf16x8 x1 = qr[8 + g], x2 = qr[10 + g];
; #pragma unroll
;                 for (int e = 0; e < 8; ++e) { const f32x2 cs = rt[g * 16 + hi * 8 + e];
;                     const float a = bf2f((unsigned short)x1[e]), c = bf2f((unsigned short)x2[e]);
;                     const float ra = a * cs.x - c * cs.y, rc = c * cs.x + a * cs.y;
;                     x1[e] = (short)(cvt_pk_bf16(ra, 0.f) & 0xffffu); x2[e] = (short)(cvt_pk_bf16(rc, 0.f) & 0xffffu); }
;                 qr[8 + g] = x1; qr[10 + g] = x2;
;             }
	v_pk_mul_f32 v[34:35], v[26:27], v[30:31] op_sel:[0,1] op_sel_hi:[1,0]
	v_pk_mul_f32 v[26:27], v[26:27], v[30:31]
	v_sub_f32_e32 v28, v34, v35
	v_add_f32_e32 v26, v26, v27
	v_cvt_pk_bf16_f32 v27, v28, v193
	v_cvt_pk_bf16_f32 v26, v26, v193
	global_load_dwordx2 v[30:31], v[8:9], off offset:56
	v_and_b32_e32 v28, 0xffff0000, v33
	v_lshlrev_b32_e32 v35, 16, v0
	v_lshlrev_b32_e32 v34, 16, v4
	s_waitcnt vmcnt(0)
	v_pk_mul_f32 v[32:33], v[30:31], v[28:29] op_sel:[0,1] op_sel_hi:[1,0]
	v_pk_mul_f32 v[28:29], v[30:31], v[28:29]
	v_sub_f32_e32 v32, v32, v33
	v_add_f32_e32 v28, v28, v29
	v_cvt_pk_bf16_f32 v30, v32, v193
	v_cvt_pk_bf16_f32 v28, v28, v193
	global_load_dwordx2 v[32:33], v[8:9], off offset:128
	s_waitcnt vmcnt(0)
	v_pk_mul_f32 v[36:37], v[32:33], v[34:35] op_sel:[0,1] op_sel_hi:[1,0]
	v_pk_mul_f32 v[32:33], v[32:33], v[34:35]
	v_sub_f32_e32 v29, v36, v37
	v_add_f32_e32 v32, v32, v33
	v_cvt_pk_bf16_f32 v31, v29, v193
	v_cvt_pk_bf16_f32 v29, v32, v193
	global_load_dwordx2 v[32:33], v[8:9], off offset:136
	v_and_b32_e32 v35, 0xffff0000, v0
	v_and_b32_e32 v34, 0xffff0000, v4
	s_waitcnt vmcnt(0)
	v_pk_mul_f32 v[36:37], v[32:33], v[34:35] op_sel:[0,1] op_sel_hi:[1,0]
	v_pk_mul_f32 v[32:33], v[32:33], v[34:35]
	v_sub_f32_e32 v0, v36, v37
	v_add_f32_e32 v4, v32, v33
	v_cvt_pk_bf16_f32 v32, v0, v193
	v_cvt_pk_bf16_f32 v4, v4, v193
	global_load_dwordx2 v[34:35], v[8:9], off offset:144
	v_lshlrev_b32_e32 v37, 16, v1
	v_lshlrev_b32_e32 v36, 16, v5
	v_and_b32_e32 v1, 0xffff0000, v1
	s_waitcnt vmcnt(0)
	v_pk_mul_f32 v[38:39], v[34:35], v[36:37] op_sel:[0,1] op_sel_hi:[1,0]
	v_pk_mul_f32 v[34:35], v[34:35], v[36:37]
	v_sub_f32_e32 v0, v38, v39
	v_add_f32_e32 v33, v34, v35
	v_cvt_pk_bf16_f32 v34, v0, v193
	v_cvt_pk_bf16_f32 v33, v33, v193
	global_load_dwordx2 v[36:37], v[8:9], off offset:152
	v_and_b32_e32 v0, 0xffff0000, v5
	s_waitcnt vmcnt(0)
	v_pk_mul_f32 v[38:39], v[36:37], v[0:1] op_sel:[0,1] op_sel_hi:[1,0]
	v_pk_mul_f32 v[0:1], v[36:37], v[0:1]
	v_sub_f32_e32 v5, v38, v39
	v_add_f32_e32 v0, v0, v1
	v_cvt_pk_bf16_f32 v35, v5, v193
	v_cvt_pk_bf16_f32 v5, v0, v193
	global_load_dwordx2 v[0:1], v[8:9], off offset:160
	v_lshlrev_b32_e32 v37, 16, v2
	v_lshlrev_b32_e32 v36, 16, v6
	s_waitcnt vmcnt(0)
	v_pk_mul_f32 v[38:39], v[0:1], v[36:37] op_sel:[0,1] op_sel_hi:[1,0]
	v_pk_mul_f32 v[0:1], v[0:1], v[36:37]
	v_sub_f32_e32 v38, v38, v39
	v_add_f32_e32 v0, v0, v1
	v_cvt_pk_bf16_f32 v37, v38, v193
	v_cvt_pk_bf16_f32 v36, v0, v193
	global_load_dwordx2 v[0:1], v[8:9], off offset:168
	v_and_b32_e32 v39, 0xffff0000, v2
	v_and_b32_e32 v38, 0xffff0000, v6
	s_waitcnt vmcnt(0)
	v_pk_mul_f32 v[40:41], v[0:1], v[38:39] op_sel:[0,1] op_sel_hi:[1,0]
	v_pk_mul_f32 v[0:1], v[0:1], v[38:39]
	v_sub_f32_e32 v2, v40, v41
	v_add_f32_e32 v0, v0, v1
	v_cvt_pk_bf16_f32 v6, v2, v193
	v_cvt_pk_bf16_f32 v2, v0, v193
	global_load_dwordx2 v[0:1], v[8:9], off offset:176
	v_lshlrev_b32_e32 v39, 16, v3
	v_lshlrev_b32_e32 v38, 16, v7
	s_waitcnt vmcnt(0)
	v_pk_mul_f32 v[40:41], v[0:1], v[38:39] op_sel:[0,1] op_sel_hi:[1,0]
	v_pk_mul_f32 v[0:1], v[0:1], v[38:39]
	v_sub_f32_e32 v40, v40, v41
	v_add_f32_e32 v0, v0, v1
	v_cvt_pk_bf16_f32 v39, v40, v193
	v_cvt_pk_bf16_f32 v38, v0, v193
	global_load_dwordx2 v[0:1], v[8:9], off offset:184
	v_and_b32_e32 v9, 0xffff0000, v3
	v_and_b32_e32 v8, 0xffff0000, v7
	s_waitcnt vmcnt(0)
; #define VM_WAIT() asm volatile("s_waitcnt vmcnt(0)" ::: "memory")
; __device__ __forceinline__ unsigned cvt_pk_bf16(float lo, float hi) { unsigned r; asm volatile("v_cvt_pk_bf16_f32 %0, %1, %2" : "=v"(r) : "v"(lo), "v"(hi)); return r; }
;     ...
;                 bf16x8 x1 = qr[8 + g], x2 = qr[10 + g];
; #pragma unroll
;                 for (int e = 0; e < 8; ++e) { const f32x2 cs = rt[g * 16 + hi * 8 + e];
;                     const float a = bf2f((unsigned short)x1[e]), c = bf2f((unsigned short)x2[e]);
;                     const float ra = a * cs.x - c * cs.y, rc = c * cs.x + a * cs.y;
;                     x1[e] = (short)(cvt_pk_bf16(ra, 0.f) & 0xffffu); x2[e] = (short)(cvt_pk_bf16(rc, 0.f) & 0xffffu); }
;                 qr[8 + g] = x1; qr[10 + g] = x2;
;             }
;     ...
;         unsigned gsv[2], gsk[2], gsk2 = 0u;
; #pragma unroll
;         for (int i = 0; i < 2; ++i) { const int a = (i * 512 + tid) * 16;
;             { const int sub = a >> 9, within = a & 511; const int kk = (sub >> 2) * 8 + (within >> 6); const int k = (kk & ~0xC) | ((kk & 4) << 1) | ((kk & 8) >> 1);
;               const int c = (sub & 3) * 32 + ((within & 63) >> 1); gsv[i] = (unsigned)(k * ldv + c) * 2u; }
;             if constexpr (MODE == MODE_DIFF) { if (i == 0) { const int row = a >> 7, ch = ((a >> 4) & 7) ^ ((row >> 1) & 7); gsk[0] = (unsigned)(row * ldk + ch * 8) * 2u; } gsk[1] = 0u; }
;             else { const int row = a >> 8, ch = ((a >> 4) & 15) ^ (row & 15); gsk[i] = (unsigned)(row * ldk + ch * 8) * 2u; } }
;         if constexpr (MODE == MODE_MLA) { const int a = tid * 16, row = a >> 7, ch = ((a >> 4) & 7) ^ ((row >> 1) & 7); gsk2 = (unsigned)(row * UW + ch * 8) * 2u; }
;         const unsigned ldsw = (unsigned)__builtin_amdgcn_readfirstlane(wid) * 1024u;
;     ...
;         GLDS(0, 0); VM_WAIT(); __syncthreads();
	v_pk_mul_f32 v[40:41], v[0:1], v[8:9] op_sel:[0,1] op_sel_hi:[1,0]
	v_pk_mul_f32 v[0:1], v[0:1], v[8:9]
	v_sub_f32_e32 v3, v40, v41
	v_add_f32_e32 v0, v0, v1
	v_bfe_i32 v9, v11, 4, 24
	v_cvt_pk_bf16_f32 v8, v3, v193
	v_cvt_pk_bf16_f32 v7, v0, v193
	v_bfe_u32 v0, v11, 2, 2
	v_lshrrev_b32_e32 v1, 1, v11
	v_lshlrev_b32_e32 v3, 1, v11
	v_lshrrev_b32_e32 v41, 1, v9
	v_and_or_b32 v0, v1, 8, v0
	v_and_b32_e32 v1, 0xc0, v3
	v_and_b32_e32 v40, 0xffff0, v9
	v_and_b32_e32 v41, 4, v41
	v_and_or_b32 v1, v13, 48, v1
	v_or3_b32 v40, v40, v41, v0
	v_lshl_or_b32 v192, v40, 12, v1
	v_xor_b32_e32 v40, v9, v11
	v_lshlrev_b32_e32 v9, 12, v9
	v_lshlrev_b32_e32 v40, 4, v40
	v_and_or_b32 v146, v40, s87, v9
	v_add_u32_e32 v9, 0x2000, v13
	v_ashrrev_i32_e32 v9, 8, v9
	v_lshrrev_b32_e32 v41, 1, v9
	v_and_b32_e32 v40, 0xffff0, v9
	v_and_b32_e32 v41, 4, v41
	v_or3_b32 v0, v40, v41, v0
	v_lshl_add_u64 v[40:41], s[0:1], 0, v[192:193]
	v_lshl_or_b32 v148, v0, 12, v1
	v_lshl_add_u64 v[40:41], v[40:41], 0, s[36:37]
	global_load_lds_dwordx4 v[40:41], off
	v_lshl_add_u64 v[40:41], s[0:1], 0, v[148:149]
	v_xor_b32_e32 v0, v9, v11
	v_lshl_add_u64 v[40:41], v[40:41], 0, s[36:37]
	s_add_i32 m0, s29, 0x2000
	v_lshlrev_b32_e32 v1, 12, v9
	v_lshlrev_b32_e32 v0, 4, v0
	global_load_lds_dwordx4 v[40:41], off
	s_mov_b32 m0, s2
	v_and_or_b32 v150, v0, s87, v1
	global_load_lds_dwordx4 v146, s[0:1]
	s_add_i32 m0, s29, 0xe000
	v_lshlrev_b32_e32 v0, 10, v11
	global_load_lds_dwordx4 v150, s[0:1]
	s_lshl_b64 s[0:1], s[4:5], 13
	v_and_b32_e32 v0, 0xffffe000, v0
	v_xor_b32_e32 v1, v13, v11
	s_add_u32 s0, s14, s0
	v_and_or_b32 v0, v1, s3, v0
	s_addc_u32 s1, s15, s1
	s_add_i32 m0, s29, 0x10000
	v_mov_b32_e32 v1, v193
	global_load_lds_dwordx4 v0, s[0:1]
	v_lshl_add_u64 v[152:153], s[14:15], 0, v[0:1]
	v_bitop3_b32 v0, v155, v11, 15 bitop3:0x78
	v_lshlrev_b32_e32 v9, 3, v11
	v_lshlrev_b32_e32 v158, 4, v0
	v_and_b32_e32 v0, 0xf0, v13
	v_bitop3_b32 v159, v144, v0, 32 bitop3:0x36
	v_bitop3_b32 v160, v144, v0, 64 bitop3:0x36
	v_bitop3_b32 v161, v144, v0, s60 bitop3:0x36
	v_bitop3_b32 v162, v144, v0, s59 bitop3:0x36
	v_bitop3_b32 v164, v144, v0, s61 bitop3:0x36
	v_bitop3_b32 v165, v144, v0, s58 bitop3:0x36
	v_bitop3_b32 v166, v144, v0, s62 bitop3:0x36
	v_and_b32_e32 v0, 0x70, v9
	v_bitop3_b32 v169, v144, v0, 32 bitop3:0x36
	v_bitop3_b32 v170, v144, v0, 64 bitop3:0x36
	v_bitop3_b32 v171, v144, v0, s60 bitop3:0x36
	v_and_b32_e32 v0, 0x118, v9
	s_mov_b32 s0, 0x5040100
	s_waitcnt vmcnt(0)
	v_perm_b32 v128, v17, v15, s0
	v_perm_b32 v136, v16, v14, s0
	v_and_or_b32 v0, v3, 32, v0
	v_mov_b32_e32 v14, v193
	v_mov_b32_e32 v15, v193
	v_bitop3_b32 v168, v144, v9, s3 bitop3:0x78
	v_cmp_gt_u32_e64 s[2:3], 32, v10
	v_perm_b32 v129, v21, v19, s0
	v_perm_b32 v130, v25, v23, s0
	v_perm_b32 v131, v30, v27, s0
	v_perm_b32 v132, v32, v31, s0
	v_perm_b32 v133, v35, v34, s0
	v_perm_b32 v134, v6, v37, s0
	v_perm_b32 v135, v8, v39, s0
	v_perm_b32 v137, v20, v18, s0
	v_perm_b32 v138, v24, v22, s0
	v_perm_b32 v139, v28, v26, s0
	v_perm_b32 v140, v4, v29, s0
	v_perm_b32 v141, v5, v33, s0
	v_perm_b32 v142, v2, v36, s0
	v_perm_b32 v143, v7, v38, s0
	v_add3_u32 v172, v12, 0, v0
	v_mov_b32_e32 v0, v193
	v_mov_b32_e32 v2, v193
	v_mov_b32_e32 v3, v193
	v_mov_b32_e32 v4, v193
	v_mov_b32_e32 v5, v193
	v_mov_b32_e32 v6, v193
	v_mov_b32_e32 v7, v193
	v_mov_b32_e32 v8, v193
	v_mov_b32_e32 v9, v193
	v_mov_b32_e32 v10, v193
	v_mov_b32_e32 v11, v193
	v_mov_b32_e32 v12, v193
	v_mov_b32_e32 v13, v193
	v_mov_b64_e32 v[30:31], v[14:15]
	v_mov_b64_e32 v[46:47], v[14:15]
	v_mov_b64_e32 v[62:63], v[14:15]
	s_or_b32 s16, s4, 64
	v_mov_b64_e32 v[28:29], v[12:13]
	v_mov_b64_e32 v[26:27], v[10:11]
	v_mov_b64_e32 v[24:25], v[8:9]
	v_mov_b64_e32 v[22:23], v[6:7]
	v_mov_b64_e32 v[20:21], v[4:5]
	v_mov_b64_e32 v[18:19], v[2:3]
	v_mov_b64_e32 v[16:17], v[0:1]
	v_mov_b64_e32 v[44:45], v[12:13]
	v_mov_b64_e32 v[42:43], v[10:11]
	v_mov_b64_e32 v[40:41], v[8:9]
	v_mov_b64_e32 v[38:39], v[6:7]
	v_mov_b64_e32 v[36:37], v[4:5]
	v_mov_b64_e32 v[34:35], v[2:3]
	v_mov_b64_e32 v[32:33], v[0:1]
	v_mov_b64_e32 v[60:61], v[12:13]
	v_mov_b64_e32 v[58:59], v[10:11]
	v_mov_b64_e32 v[56:57], v[8:9]
	v_mov_b64_e32 v[54:55], v[6:7]
	v_mov_b64_e32 v[52:53], v[4:5]
	v_mov_b64_e32 v[50:51], v[2:3]
	v_mov_b64_e32 v[48:49], v[0:1]
	s_waitcnt vmcnt(0) lgkmcnt(0)
	s_barrier
	s_and_b32 s30, s28, 1
	s_cmp_eq_u32 s28, 63
	s_cbranch_scc1 .LBB0_788
	s_branch .LBB0_787

; #define LAS __attribute__((address_space(3)))
; __device__ __forceinline__ void cvt_finish(const CvtDesc& d, const float (&t)[64], LAS float* scr, int lane) {
;     LAS float* sw = scr + (lane >> 4) * 65 + 4 * (lane & 15);
; #pragma unroll
;     for (int i = 0; i < 16; ++i) { sw[(4 * i) * 65] = t[4 * i]; sw[(4 * i) * 65 + 1] = t[4 * i + 1]; sw[(4 * i) * 65 + 2] = t[4 * i + 2]; sw[(4 * i) * 65 + 3] = t[4 * i + 3]; }
;     LDS_WAIT();
;     const int c = lane & 7;
;     if (d.f8) {
; #pragma unroll
;         for (int j = 0; j < 8; ++j) { const int n = (lane >> 3) + 8 * j; const LAS float* s = scr + (8 * c) * 65 + n;
;             int a = __builtin_amdgcn_cvt_pk_fp8_f32(clamp8(s[0 * 65] * W8_SCALE), clamp8(s[1 * 65] * W8_SCALE), 0, false); a = __builtin_amdgcn_cvt_pk_fp8_f32(clamp8(s[2 * 65] * W8_SCALE), clamp8(s[3 * 65] * W8_SCALE), a, true);
;             int b = __builtin_amdgcn_cvt_pk_fp8_f32(clamp8(s[4 * 65] * W8_SCALE), clamp8(s[5 * 65] * W8_SCALE), 0, false); b = __builtin_amdgcn_cvt_pk_fp8_f32(clamp8(s[6 * 65] * W8_SCALE), clamp8(s[7 * 65] * W8_SCALE), b, true);
; __device__ __forceinline__ CvtDesc conv_expert_desc(const KA& a, unsigned char* ws, int q) {
;     const int l = q / Q_PER_L; int r = q - l * Q_PER_L;
;     unsigned char* wl = ws + WS_W + (size_t)l * W_LSTRIDE;
;     CvtDesc d; d.f8 = (MOE_FP8_LAST && (MOE_FP8_GU_ALL || l == NLAYER - 1)) ? 1 : 0;
;     if (MOE_FP8_LAST && MOE_FP8_DOWN_ALL && r >= 2 * Q_IG) d.f8 = 1;
;     const int eb = d.f8 ? 1 : 2;
;     if (r < 2 * Q_IG) { const int up = r >= Q_IG; if (up) r -= Q_IG; const int e = r >> 8, rr = r & 255, kb = rr >> 3, nb = rr & 7, n0 = nb * 64;
;         const float* src = e < 64 ? a.in(up ? 21 : 20) + ((size_t)l * 64 + e) * DM * FFE : a.in(up ? 24 : 23) + (size_t)l * DM * FFE;
;         d.src = src + (size_t)(kb * 64) * FFE + n0; d.N = FFE; d.dKB = DM * eb;
;         d.dst = wl + W_GU + ((size_t)e * 1024 * DM + (size_t)((n0 >> 7) * 256 + up * 128 + (n0 & 127)) * DM + kb * 64) * eb;
;     } else { r -= 2 * Q_IG; const int e = r >> 8, rr = r & 255, kb = rr >> 5, nb = rr & 31;
;         const float* src = e < 64 ? a.in(22) + ((size_t)l * 64 + e) * FFE * DM : a.in(25) + (size_t)l * FFE * DM;
;         d.src = src + (size_t)(kb * 64) * DM + nb * 64; d.N = DM; d.dKB = FFE * eb;
;         d.dst = wl + W_D + ((size_t)e * DM * FFE + (size_t)(nb * 64) * FFE + kb * 64) * eb; }
;     return d;
; }
.LBB0_788:
	s_and_b32 s49, s28, 3
	s_lshr_b32 s46, s28, 2
	s_sub_u32 s46, s28, s46
	s_cmp_lg_u32 s49, 3
	s_cselect_b32 s50, 1, 0
	s_cmp_eq_u32 s28, 3
	s_cselect_b32 s46, 48, s46
	s_cselect_b32 s50, 1, s50
	s_lshl_b32 s49, s46, 2
	s_add_u32 s49, s49, s54
	s_cmp_lt_u32 s49, 0xc3
	s_cselect_b32 s100, 1, 0
	s_and_b32 s50, s50, s100
	s_cmp_eq_u32 s50, 0
	s_cbranch_scc1 .Lilc_proc
	s_lshr_b32 s55, s46, 4
	s_and_b32 s57, s49, 63
	s_lshl_b32 s101, s56, 6
	s_add_u32 s101, s101, s57
	s_cmp_eq_u32 s55, 3
	s_cselect_b32 s55, s54, s55
	s_cselect_b32 s100, 3, 0
	s_cselect_b32 s101, s56, s101
	s_cselect_b32 s57, 64, s57
	s_add_u32 s100, s100, s55
	s_lshl_b32 s100, s100, 3
	s_add_u32 s100, s100, 0xa0
	s_load_dwordx2 s[44:45], s[6:7], s100
.Lilc_proc:
	s_cmp_eq_u32 s42, 0
	s_cbranch_scc1 .Lilc_noproc
	v_mul_f32_e32 v232, 0x42800000, v232
	v_mul_f32_e32 v233, 0x42800000, v233
	v_mul_f32_e32 v234, 0x42800000, v234
	v_mul_f32_e32 v235, 0x42800000, v235
	v_mul_f32_e32 v236, 0x42800000, v236
	v_mul_f32_e32 v237, 0x42800000, v237
	v_mul_f32_e32 v238, 0x42800000, v238
	v_mul_f32_e32 v239, 0x42800000, v239
	v_mul_f32_e32 v240, 0x42800000, v240
	v_mul_f32_e32 v241, 0x42800000, v241
	v_mul_f32_e32 v242, 0x42800000, v242
	v_mul_f32_e32 v243, 0x42800000, v243
	v_mul_f32_e32 v244, 0x42800000, v244
	v_mul_f32_e32 v245, 0x42800000, v245
	v_mul_f32_e32 v246, 0x42800000, v246
	v_mul_f32_e32 v247, 0x42800000, v247
	v_mul_f32_e32 v248, 0x42800000, v248
	v_mul_f32_e32 v249, 0x42800000, v249
	v_mul_f32_e32 v250, 0x42800000, v250
	v_mul_f32_e32 v251, 0x42800000, v251
	v_mul_f32_e32 v206, 0x42800000, v206
	v_mul_f32_e32 v207, 0x42800000, v207
	v_mul_f32_e32 v208, 0x42800000, v208
	v_mul_f32_e32 v209, 0x42800000, v209
	v_mul_f32_e32 v210, 0x42800000, v210
	v_mul_f32_e32 v211, 0x42800000, v211
	v_mul_f32_e32 v212, 0x42800000, v212
	v_mul_f32_e32 v213, 0x42800000, v213
	v_mul_f32_e32 v214, 0x42800000, v214
	v_mul_f32_e32 v215, 0x42800000, v215
	v_mul_f32_e32 v216, 0x42800000, v216
	v_mul_f32_e32 v217, 0x42800000, v217
	v_med3_f32 v232, v232, s93, v224
	v_med3_f32 v233, v233, s93, v224
	v_med3_f32 v234, v234, s93, v224
	v_med3_f32 v235, v235, s93, v224
	v_med3_f32 v236, v236, s93, v224
	v_med3_f32 v237, v237, s93, v224
	v_med3_f32 v238, v238, s93, v224
	v_med3_f32 v239, v239, s93, v224
	v_med3_f32 v240, v240, s93, v224
	v_med3_f32 v241, v241, s93, v224
	v_med3_f32 v242, v242, s93, v224
	v_med3_f32 v243, v243, s93, v224
	v_med3_f32 v244, v244, s93, v224
	v_med3_f32 v245, v245, s93, v224
	v_med3_f32 v246, v246, s93, v224
	v_med3_f32 v247, v247, s93, v224
	v_med3_f32 v248, v248, s93, v224
	v_med3_f32 v249, v249, s93, v224
	v_med3_f32 v250, v250, s93, v224
	v_med3_f32 v251, v251, s93, v224
	v_med3_f32 v206, v206, s93, v224
	v_med3_f32 v207, v207, s93, v224
	v_med3_f32 v208, v208, s93, v224
	v_med3_f32 v209, v209, s93, v224
	v_med3_f32 v210, v210, s93, v224
	v_med3_f32 v211, v211, s93, v224
	v_med3_f32 v212, v212, s93, v224
	v_med3_f32 v213, v213, s93, v224
	v_med3_f32 v214, v214, s93, v224
	v_med3_f32 v215, v215, s93, v224
	v_med3_f32 v216, v216, s93, v224
	v_med3_f32 v217, v217, s93, v224
	v_lshlrev_b32_e32 v230, 3, v226
	v_lshl_add_u32 v225, v229, s42, v230
	v_cvt_pk_fp8_f32 v252, v232, v236
	v_cvt_pk_fp8_f32 v253, v248, v206
	v_cvt_pk_fp8_f32 v252, v240, v244 op_sel:[0,0,1]
	v_cvt_pk_fp8_f32 v253, v210, v214 op_sel:[0,0,1]
	s_nop 0
	global_store_dwordx2 v225, v[252:253], s[40:41]
	v_add_u32_e32 v225, s43, v225
	v_cvt_pk_fp8_f32 v252, v233, v237
	v_cvt_pk_fp8_f32 v253, v249, v207
	v_cvt_pk_fp8_f32 v252, v241, v245 op_sel:[0,0,1]
	v_cvt_pk_fp8_f32 v253, v211, v215 op_sel:[0,0,1]
	s_nop 0
	global_store_dwordx2 v225, v[252:253], s[40:41]
	v_add_u32_e32 v225, s43, v225
	v_cvt_pk_fp8_f32 v252, v234, v238
	v_cvt_pk_fp8_f32 v253, v250, v208
	v_cvt_pk_fp8_f32 v252, v242, v246 op_sel:[0,0,1]
	v_cvt_pk_fp8_f32 v253, v212, v216 op_sel:[0,0,1]
	s_nop 0
	global_store_dwordx2 v225, v[252:253], s[40:41]
	v_add_u32_e32 v225, s43, v225
	v_cvt_pk_fp8_f32 v252, v235, v239
	v_cvt_pk_fp8_f32 v253, v251, v209
	v_cvt_pk_fp8_f32 v252, v243, v247 op_sel:[0,0,1]
	v_cvt_pk_fp8_f32 v253, v213, v217 op_sel:[0,0,1]
	s_nop 0
	global_store_dwordx2 v225, v[252:253], s[40:41]
.Lilc_noproc:
	s_mov_b32 s42, 0
	s_cmp_eq_u32 s50, 0
	s_cbranch_scc1 .Lilc_done
	s_waitcnt lgkmcnt(0)
	s_lshr_b32 s49, s101, 10
	s_lshl_b32 s101, s101, 22
	s_add_u32 s44, s44, s101
	s_addc_u32 s45, s45, s49
	s_cmp_eq_u32 s55, 2
	s_cbranch_scc1 .Lilc_down
	s_lshr_b32 s49, s39, 4
	s_and_b32 s46, s39, 15
	s_lshl_b32 s100, s49, 17
	s_lshl_b32 s101, s46, 7
	s_add_u32 s100, s100, s101
	s_add_u32 s44, s44, s100
	s_addc_u32 s45, s45, 0
	s_lshr_b32 s100, s46, 2
	s_lshl_b32 s100, s100, 8
	s_lshl_b32 s101, s55, 7
	s_add_u32 s100, s100, s101
	s_and_b32 s101, s46, 3
	s_lshl_b32 s101, s101, 5
	s_add_u32 s100, s100, s101
	s_lshl_b32 s100, s100, 11
	s_lshl_b32 s101, s49, 6
	s_add_u32 s100, s100, s101
	s_lshl_b32 s101, s57, 21
	s_add_u32 s100, s100, s101
	s_add_u32 s100, s100, 0x34000000
	s_mul_i32 s101, s56, 0x1a800000
	s_add_u32 s100, s100, s101
	s_add_u32 s40, s8, s100
	s_addc_u32 s41, s9, 0
	s_mov_b32 s42, 13
	s_movk_i32 s43, 0x800
	s_movk_i32 s47, 0x800
	s_mov_b32 s48, 14
	s_branch .Lilc_issue
.Lilc_down:
	s_lshr_b32 s49, s39, 6
	s_and_b32 s46, s39, 63
	s_lshl_b32 s100, s49, 19
	s_lshl_b32 s101, s46, 7
	s_add_u32 s100, s100, s101
	s_add_u32 s44, s44, s100
	s_addc_u32 s45, s45, 0
	s_lshl_b32 s100, s46, 14
	s_lshl_b32 s101, s49, 6
	s_add_u32 s100, s100, s101
	s_lshl_b32 s101, s57, 20
	s_add_u32 s100, s100, s101
	s_add_u32 s100, s100, 0x44400000
	s_mul_i32 s101, s56, 0x1a800000
	s_add_u32 s100, s100, s101
	s_add_u32 s40, s8, s100
	s_addc_u32 s41, s9, 0
	s_mov_b32 s42, 11
	s_movk_i32 s43, 0x200
	s_movk_i32 s47, 0x2000
	s_mov_b32 s48, 16
.Lilc_issue:
	v_lshlrev_b32_e32 v230, 4, v229
	v_lshl_add_u32 v223, v226, s48, v230
	global_load_dwordx4 v[232:235], v223, s[44:45] nt
	v_add_u32_e32 v223, s47, v223
	global_load_dwordx4 v[236:239], v223, s[44:45] nt
	v_add_u32_e32 v223, s47, v223
	global_load_dwordx4 v[240:243], v223, s[44:45] nt
	v_add_u32_e32 v223, s47, v223
	global_load_dwordx4 v[244:247], v223, s[44:45] nt
	v_add_u32_e32 v223, s47, v223
	global_load_dwordx4 v[248:251], v223, s[44:45] nt
	v_add_u32_e32 v223, s47, v223
	global_load_dwordx4 v[206:209], v223, s[44:45] nt
	v_add_u32_e32 v223, s47, v223
	global_load_dwordx4 v[210:213], v223, s[44:45] nt
	v_add_u32_e32 v223, s47, v223
	global_load_dwordx4 v[214:217], v223, s[44:45] nt
